# g23: g22 + P1 epilogue (in-projection output, 369 MB) stored non-temporal so XN1/WinT are not displaced from the memory-side cache during P1
# baseline (speedup 1.0000x reference)
.LBB0_89:
	v_lshl_or_b32 v148, s48, 8, v155
	v_lshl_add_u32 v169, s24, 8, v154
	v_ashrrev_i32_e32 v149, 31, v148
	v_mov_b64_e32 v[146:147], s[10:11]
	v_mad_i64_i32 v[170:171], s[26:27], v169, s56, v[146:147]
	v_lshlrev_b64 v[148:149], 1, v[148:149]
	v_lshl_add_u64 v[170:171], v[170:171], 0, v[148:149]
	v_cvt_pk_bf16_f32 v126, v126, v127
	v_cvt_pk_bf16_f32 v127, v128, v129
	v_cvt_pk_bf16_f32 v128, v122, v123
	v_cvt_pk_bf16_f32 v129, v124, v125
	global_store_dwordx4 v[170:171], v[126:129], off nt
	v_cvt_pk_bf16_f32 v114, v114, v115
	v_cvt_pk_bf16_f32 v115, v116, v117
	v_cvt_pk_bf16_f32 v116, v106, v107
	v_or_b32_e32 v106, 16, v169
	v_mad_i64_i32 v[106:107], s[26:27], v106, s56, v[146:147]
	v_cvt_pk_bf16_f32 v117, v108, v109
	global_store_dwordx4 v[170:171], v[114:117], off offset:256 nt
	s_andn2_b64 vcc, exec, s[4:5]
	s_mov_b64 s[4:5], -1
	v_lshl_add_u64 v[114:115], v[106:107], 0, v[148:149]
	v_cvt_pk_bf16_f32 v106, v118, v119
	v_cvt_pk_bf16_f32 v107, v120, v121
	v_cvt_pk_bf16_f32 v108, v110, v111
	v_cvt_pk_bf16_f32 v109, v112, v113
	global_store_dwordx4 v[114:115], v[106:109], off nt
	v_cvt_pk_bf16_f32 v98, v98, v99
	v_cvt_pk_bf16_f32 v99, v100, v101
	v_cvt_pk_bf16_f32 v100, v90, v91
	v_or_b32_e32 v90, 32, v169
	v_mad_i64_i32 v[90:91], s[26:27], v90, s56, v[146:147]
	v_cvt_pk_bf16_f32 v101, v92, v93
	global_store_dwordx4 v[114:115], v[98:101], off offset:256 nt
	s_nop 1
	v_lshl_add_u64 v[98:99], v[90:91], 0, v[148:149]
	v_cvt_pk_bf16_f32 v90, v102, v103
	v_cvt_pk_bf16_f32 v91, v104, v105
	v_cvt_pk_bf16_f32 v92, v94, v95
	v_cvt_pk_bf16_f32 v93, v96, v97
	global_store_dwordx4 v[98:99], v[90:93], off nt
	v_cvt_pk_bf16_f32 v82, v82, v83
	v_cvt_pk_bf16_f32 v83, v84, v85
	v_cvt_pk_bf16_f32 v84, v74, v75
	v_or_b32_e32 v74, 48, v169
	v_mad_i64_i32 v[74:75], s[26:27], v74, s56, v[146:147]
	v_cvt_pk_bf16_f32 v85, v76, v77
	global_store_dwordx4 v[98:99], v[82:85], off offset:256 nt
	s_nop 1
	v_lshl_add_u64 v[82:83], v[74:75], 0, v[148:149]
	v_cvt_pk_bf16_f32 v74, v86, v87
	v_cvt_pk_bf16_f32 v75, v88, v89
	v_cvt_pk_bf16_f32 v76, v78, v79
	v_cvt_pk_bf16_f32 v77, v80, v81
	global_store_dwordx4 v[82:83], v[74:77], off nt
	v_cvt_pk_bf16_f32 v70, v70, v71
	v_cvt_pk_bf16_f32 v71, v72, v73
	v_cvt_pk_bf16_f32 v72, v66, v67
	v_add_u32_e32 v66, 0x80, v169
	v_mad_i64_i32 v[66:67], s[26:27], v66, s56, v[146:147]
	v_lshl_add_u64 v[66:67], v[66:67], 0, v[148:149]
	v_cvt_pk_bf16_f32 v73, v68, v69
	global_store_dwordx4 v[82:83], v[70:73], off offset:256 nt
	v_cvt_pk_bf16_f32 v62, v62, v63
	v_cvt_pk_bf16_f32 v63, v64, v65
	v_cvt_pk_bf16_f32 v64, v58, v59
	v_cvt_pk_bf16_f32 v65, v60, v61
	global_store_dwordx4 v[66:67], v[62:65], off nt
	v_cvt_pk_bf16_f32 v50, v50, v51
	v_cvt_pk_bf16_f32 v51, v52, v53
	v_cvt_pk_bf16_f32 v52, v42, v43
	v_add_u32_e32 v42, 0x90, v169
	v_mad_i64_i32 v[42:43], s[26:27], v42, s56, v[146:147]
	v_cvt_pk_bf16_f32 v53, v44, v45
	global_store_dwordx4 v[66:67], v[50:53], off offset:256 nt
	s_nop 1
	v_lshl_add_u64 v[50:51], v[42:43], 0, v[148:149]
	v_cvt_pk_bf16_f32 v42, v54, v55
	v_cvt_pk_bf16_f32 v43, v56, v57
	v_cvt_pk_bf16_f32 v44, v46, v47
	v_cvt_pk_bf16_f32 v45, v48, v49
	global_store_dwordx4 v[50:51], v[42:45], off nt
	v_cvt_pk_bf16_f32 v34, v34, v35
	v_cvt_pk_bf16_f32 v35, v36, v37
	v_cvt_pk_bf16_f32 v36, v26, v27
	v_add_u32_e32 v26, 0xa0, v169
	v_mad_i64_i32 v[26:27], s[26:27], v26, s56, v[146:147]
	v_cvt_pk_bf16_f32 v37, v28, v29
	global_store_dwordx4 v[50:51], v[34:37], off offset:256 nt
	s_nop 1
	v_lshl_add_u64 v[34:35], v[26:27], 0, v[148:149]
	v_cvt_pk_bf16_f32 v26, v38, v39
	v_cvt_pk_bf16_f32 v27, v40, v41
	v_cvt_pk_bf16_f32 v28, v30, v31
	v_cvt_pk_bf16_f32 v29, v32, v33
	global_store_dwordx4 v[34:35], v[26:29], off nt
	v_cvt_pk_bf16_f32 v18, v18, v19
	v_cvt_pk_bf16_f32 v19, v20, v21
	v_cvt_pk_bf16_f32 v20, v10, v11
	v_add_u32_e32 v10, 0xb0, v169
	v_mad_i64_i32 v[10:11], s[26:27], v10, s56, v[146:147]
	v_cvt_pk_bf16_f32 v21, v12, v13
	global_store_dwordx4 v[34:35], v[18:21], off offset:256 nt
	s_nop 1
	v_lshl_add_u64 v[18:19], v[10:11], 0, v[148:149]
	v_cvt_pk_bf16_f32 v10, v22, v23
	v_cvt_pk_bf16_f32 v11, v24, v25
	v_cvt_pk_bf16_f32 v12, v14, v15
	v_cvt_pk_bf16_f32 v13, v16, v17
	global_store_dwordx4 v[18:19], v[10:13], off nt
	v_cvt_pk_bf16_f32 v6, v6, v7
	v_cvt_pk_bf16_f32 v7, v8, v9
	v_cvt_pk_bf16_f32 v8, v2, v3
	v_cvt_pk_bf16_f32 v9, v4, v5
	global_store_dwordx4 v[18:19], v[6:9], off offset:256 nt
	s_cbranch_vccnz .LBB0_82
	s_andn2_b64 vcc, exec, s[8:9]
	s_cbranch_vccnz .LBB0_81
	s_barrier
	s_branch .LBB0_81
